# v10 plus static s_setprio 1 for waves 4-7 during the mixers phase (SIMD partners out of lockstep)
# baseline (speedup 1.0000x reference)
.Lmy_q1:
	s_or_b64 exec, exec, s[6:7]
	s_mov_b64 s[6:7], -1
	v_readfirstlane_b32 s4, v146
	s_ashr_i32 s4, s4, 6
	s_cmp_gt_u32 s4, 3
	s_cbranch_scc0 .Lmy_prio_lo
	s_setprio 1
.Lmy_prio_lo:
	v_and_b32_e32 v245, 63, v146
	s_cmp_le_i32 s78, s1
	s_cbranch_scc0 .LBB0_891
	s_cmp_ge_i32 s1, s79
	s_cbranch_scc0 .LBB0_541
	v_readlane_b32 s5, v255, 42
	s_cmp_ge_i32 s1, s5
	s_cbranch_scc0 .LBB0_533
	v_readlane_b32 s5, v255, 42
	s_sub_i32 s26, s1, s5
	s_lshl_b64 s[6:7], s[26:27], 12
	v_ashrrev_i32_e32 v147, 31, v146
	v_lshl_add_u64 v[80:81], s[6:7], 0, v[146:147]
	v_lshlrev_b64 v[0:1], 5, v[80:81]
	v_lshl_add_u64 v[0:1], s[94:95], 0, v[0:1]
	global_load_dwordx4 v[72:75], v[0:1], off offset:16
	global_load_dwordx4 v[76:79], v[0:1], off
	s_mov_b64 s[6:7], 0x200
	v_lshl_add_u64 v[70:71], v[80:81], 0, s[6:7]
	v_lshlrev_b64 v[0:1], 5, v[70:71]
	v_lshl_add_u64 v[0:1], s[94:95], 0, v[0:1]
	global_load_dwordx4 v[50:53], v[0:1], off offset:16
	global_load_dwordx4 v[54:57], v[0:1], off
	s_mov_b64 s[6:7], 0x400
	v_lshl_add_u64 v[68:69], v[80:81], 0, s[6:7]
	v_lshlrev_b64 v[0:1], 5, v[68:69]
	v_lshl_add_u64 v[0:1], s[94:95], 0, v[0:1]
	global_load_dwordx4 v[36:39], v[0:1], off offset:16
	global_load_dwordx4 v[44:47], v[0:1], off
	s_mov_b64 s[6:7], 0x600
	v_lshl_add_u64 v[66:67], v[80:81], 0, s[6:7]
	v_lshlrev_b64 v[0:1], 5, v[66:67]
	v_lshl_add_u64 v[0:1], s[94:95], 0, v[0:1]
	global_load_dwordx4 v[32:35], v[0:1], off offset:16
	global_load_dwordx4 v[40:43], v[0:1], off
	s_mov_b64 s[6:7], 0x800
	v_lshl_add_u64 v[60:61], v[80:81], 0, s[6:7]
	v_lshlrev_b64 v[0:1], 5, v[60:61]
	v_lshl_add_u64 v[0:1], s[94:95], 0, v[0:1]
	global_load_dwordx4 v[8:11], v[0:1], off offset:16
	global_load_dwordx4 v[20:23], v[0:1], off
	s_mov_b64 s[6:7], 0xa00
	v_lshl_add_u64 v[62:63], v[80:81], 0, s[6:7]
	v_lshlrev_b64 v[0:1], 5, v[62:63]
	v_lshl_add_u64 v[0:1], s[94:95], 0, v[0:1]
	global_load_dwordx4 v[12:15], v[0:1], off offset:16
	global_load_dwordx4 v[24:27], v[0:1], off
	s_mov_b64 s[6:7], 0xc00
	v_lshl_add_u64 v[58:59], v[80:81], 0, s[6:7]
	v_lshlrev_b64 v[0:1], 5, v[58:59]
	v_lshl_add_u64 v[4:5], s[94:95], 0, v[0:1]
	global_load_dwordx4 v[0:3], v[4:5], off offset:16
	s_nop 0
	global_load_dwordx4 v[4:7], v[4:5], off
	s_mov_b64 s[6:7], 0xe00
	v_lshl_add_u64 v[64:65], v[80:81], 0, s[6:7]
	v_lshlrev_b64 v[16:17], 5, v[64:65]
	v_lshl_add_u64 v[28:29], s[94:95], 0, v[16:17]
	global_load_dwordx4 v[16:19], v[28:29], off offset:16
	s_nop 0
	global_load_dwordx4 v[28:31], v[28:29], off
	v_lshl_add_u64 v[80:81], v[80:81], 4, s[96:97]
	v_lshl_add_u64 v[70:71], v[70:71], 4, s[96:97]
	v_readlane_b32 s26, v255, 18
	s_mov_b64 s[6:7], 0
	s_waitcnt vmcnt(14)
	v_and_b32_sdwa v49, v78, v236 dst_sel:DWORD dst_unused:UNUSED_PAD src0_sel:WORD_1 src1_sel:DWORD
	v_and_b32_sdwa v82, v76, v236 dst_sel:DWORD dst_unused:UNUSED_PAD src0_sel:WORD_1 src1_sel:DWORD
	v_add3_u32 v49, v78, v49, s75
	v_and_b32_sdwa v78, v79, v236 dst_sel:DWORD dst_unused:UNUSED_PAD src0_sel:WORD_1 src1_sel:DWORD
	v_add3_u32 v76, v76, v82, s75
	v_and_b32_sdwa v82, v77, v236 dst_sel:DWORD dst_unused:UNUSED_PAD src0_sel:WORD_1 src1_sel:DWORD
	v_add3_u32 v78, v79, v78, s75
	v_add3_u32 v77, v77, v82, s75
	v_and_b32_e32 v78, 0xffff0000, v78
	v_and_b32_e32 v79, 0xffff0000, v77
	v_or_b32_sdwa v77, v78, v49 dst_sel:DWORD dst_unused:UNUSED_PAD src0_sel:DWORD src1_sel:WORD_1
	v_and_b32_sdwa v49, v74, v236 dst_sel:DWORD dst_unused:UNUSED_PAD src0_sel:WORD_1 src1_sel:DWORD
	v_and_b32_sdwa v78, v72, v236 dst_sel:DWORD dst_unused:UNUSED_PAD src0_sel:WORD_1 src1_sel:DWORD
	v_add3_u32 v49, v74, v49, s75
	v_and_b32_sdwa v74, v75, v236 dst_sel:DWORD dst_unused:UNUSED_PAD src0_sel:WORD_1 src1_sel:DWORD
	v_add3_u32 v72, v72, v78, s75
	v_and_b32_sdwa v78, v73, v236 dst_sel:DWORD dst_unused:UNUSED_PAD src0_sel:WORD_1 src1_sel:DWORD
	v_add3_u32 v74, v75, v74, s75
	v_add3_u32 v73, v73, v78, s75
	v_and_b32_e32 v74, 0xffff0000, v74
	v_or_b32_sdwa v76, v79, v76 dst_sel:DWORD dst_unused:UNUSED_PAD src0_sel:DWORD src1_sel:WORD_1
	v_and_b32_e32 v73, 0xffff0000, v73
	v_or_b32_sdwa v79, v74, v49 dst_sel:DWORD dst_unused:UNUSED_PAD src0_sel:DWORD src1_sel:WORD_1
	s_waitcnt vmcnt(12)
	v_and_b32_sdwa v49, v56, v236 dst_sel:DWORD dst_unused:UNUSED_PAD src0_sel:WORD_1 src1_sel:DWORD
	v_or_b32_sdwa v78, v73, v72 dst_sel:DWORD dst_unused:UNUSED_PAD src0_sel:DWORD src1_sel:WORD_1
	v_and_b32_sdwa v72, v54, v236 dst_sel:DWORD dst_unused:UNUSED_PAD src0_sel:WORD_1 src1_sel:DWORD
	v_add3_u32 v49, v56, v49, s75
	v_and_b32_sdwa v56, v57, v236 dst_sel:DWORD dst_unused:UNUSED_PAD src0_sel:WORD_1 src1_sel:DWORD
	v_add3_u32 v54, v54, v72, s75
	v_and_b32_sdwa v72, v55, v236 dst_sel:DWORD dst_unused:UNUSED_PAD src0_sel:WORD_1 src1_sel:DWORD
	v_add3_u32 v56, v57, v56, s75
	v_add3_u32 v55, v55, v72, s75
	v_and_b32_e32 v56, 0xffff0000, v56
	v_and_b32_e32 v57, 0xffff0000, v55
	v_or_b32_sdwa v55, v56, v49 dst_sel:DWORD dst_unused:UNUSED_PAD src0_sel:DWORD src1_sel:WORD_1
	v_and_b32_sdwa v49, v52, v236 dst_sel:DWORD dst_unused:UNUSED_PAD src0_sel:WORD_1 src1_sel:DWORD
	v_add3_u32 v49, v52, v49, s75
	v_and_b32_sdwa v52, v53, v236 dst_sel:DWORD dst_unused:UNUSED_PAD src0_sel:WORD_1 src1_sel:DWORD
	v_add3_u32 v52, v53, v52, s75
	v_and_b32_e32 v52, 0xffff0000, v52
	v_or_b32_sdwa v54, v57, v54 dst_sel:DWORD dst_unused:UNUSED_PAD src0_sel:DWORD src1_sel:WORD_1
	v_or_b32_sdwa v57, v52, v49 dst_sel:DWORD dst_unused:UNUSED_PAD src0_sel:DWORD src1_sel:WORD_1
	s_waitcnt vmcnt(10)
	v_and_b32_sdwa v49, v46, v236 dst_sel:DWORD dst_unused:UNUSED_PAD src0_sel:WORD_1 src1_sel:DWORD
	v_and_b32_sdwa v52, v44, v236 dst_sel:DWORD dst_unused:UNUSED_PAD src0_sel:WORD_1 src1_sel:DWORD
	v_add3_u32 v46, v46, v49, s75
	v_and_b32_sdwa v49, v47, v236 dst_sel:DWORD dst_unused:UNUSED_PAD src0_sel:WORD_1 src1_sel:DWORD
	v_add3_u32 v44, v44, v52, s75
	v_and_b32_sdwa v52, v45, v236 dst_sel:DWORD dst_unused:UNUSED_PAD src0_sel:WORD_1 src1_sel:DWORD
	v_add3_u32 v47, v47, v49, s75
	v_add3_u32 v45, v45, v52, s75
	v_and_b32_e32 v47, 0xffff0000, v47
	v_and_b32_e32 v49, 0xffff0000, v45
	v_or_b32_sdwa v45, v47, v46 dst_sel:DWORD dst_unused:UNUSED_PAD src0_sel:DWORD src1_sel:WORD_1
	v_and_b32_sdwa v47, v36, v236 dst_sel:DWORD dst_unused:UNUSED_PAD src0_sel:WORD_1 src1_sel:DWORD
	v_and_b32_sdwa v46, v38, v236 dst_sel:DWORD dst_unused:UNUSED_PAD src0_sel:WORD_1 src1_sel:DWORD
	v_add3_u32 v36, v36, v47, s75
	v_and_b32_sdwa v47, v37, v236 dst_sel:DWORD dst_unused:UNUSED_PAD src0_sel:WORD_1 src1_sel:DWORD
	v_add3_u32 v38, v38, v46, s75
	v_and_b32_sdwa v46, v39, v236 dst_sel:DWORD dst_unused:UNUSED_PAD src0_sel:WORD_1 src1_sel:DWORD
	v_add3_u32 v37, v37, v47, s75
	v_add3_u32 v39, v39, v46, s75
	v_and_b32_e32 v37, 0xffff0000, v37
	v_and_b32_e32 v39, 0xffff0000, v39
	v_or_b32_sdwa v46, v37, v36 dst_sel:DWORD dst_unused:UNUSED_PAD src0_sel:DWORD src1_sel:WORD_1
	s_waitcnt vmcnt(8)
	v_and_b32_sdwa v37, v40, v236 dst_sel:DWORD dst_unused:UNUSED_PAD src0_sel:WORD_1 src1_sel:DWORD
	v_or_b32_sdwa v47, v39, v38 dst_sel:DWORD dst_unused:UNUSED_PAD src0_sel:DWORD src1_sel:WORD_1
	v_add3_u32 v38, v40, v37, s75
	v_and_b32_sdwa v37, v43, v236 dst_sel:DWORD dst_unused:UNUSED_PAD src0_sel:WORD_1 src1_sel:DWORD
	v_and_b32_sdwa v39, v41, v236 dst_sel:DWORD dst_unused:UNUSED_PAD src0_sel:WORD_1 src1_sel:DWORD
	v_and_b32_sdwa v36, v42, v236 dst_sel:DWORD dst_unused:UNUSED_PAD src0_sel:WORD_1 src1_sel:DWORD
	v_add3_u32 v37, v43, v37, s75
	v_add3_u32 v39, v41, v39, s75
	v_add3_u32 v36, v42, v36, s75
	v_and_b32_e32 v37, 0xffff0000, v37
	v_and_b32_e32 v39, 0xffff0000, v39
	v_or_b32_sdwa v37, v37, v36 dst_sel:DWORD dst_unused:UNUSED_PAD src0_sel:DWORD src1_sel:WORD_1
	v_or_b32_sdwa v36, v39, v38 dst_sel:DWORD dst_unused:UNUSED_PAD src0_sel:DWORD src1_sel:WORD_1
	v_and_b32_sdwa v38, v34, v236 dst_sel:DWORD dst_unused:UNUSED_PAD src0_sel:WORD_1 src1_sel:DWORD
	v_add3_u32 v34, v34, v38, s75
	v_and_b32_sdwa v38, v35, v236 dst_sel:DWORD dst_unused:UNUSED_PAD src0_sel:WORD_1 src1_sel:DWORD
	v_and_b32_sdwa v39, v32, v236 dst_sel:DWORD dst_unused:UNUSED_PAD src0_sel:WORD_1 src1_sel:DWORD
	v_add3_u32 v35, v35, v38, s75
	v_add3_u32 v32, v32, v39, s75
	v_and_b32_sdwa v39, v33, v236 dst_sel:DWORD dst_unused:UNUSED_PAD src0_sel:WORD_1 src1_sel:DWORD
	v_and_b32_e32 v35, 0xffff0000, v35
	v_add3_u32 v33, v33, v39, s75
	v_or_b32_sdwa v39, v35, v34 dst_sel:DWORD dst_unused:UNUSED_PAD src0_sel:DWORD src1_sel:WORD_1
	s_waitcnt vmcnt(6)
	v_and_b32_sdwa v34, v22, v236 dst_sel:DWORD dst_unused:UNUSED_PAD src0_sel:WORD_1 src1_sel:DWORD
	v_and_b32_sdwa v35, v20, v236 dst_sel:DWORD dst_unused:UNUSED_PAD src0_sel:WORD_1 src1_sel:DWORD
	v_add3_u32 v22, v22, v34, s75
	v_and_b32_sdwa v34, v23, v236 dst_sel:DWORD dst_unused:UNUSED_PAD src0_sel:WORD_1 src1_sel:DWORD
	v_add3_u32 v20, v20, v35, s75
	v_and_b32_sdwa v35, v21, v236 dst_sel:DWORD dst_unused:UNUSED_PAD src0_sel:WORD_1 src1_sel:DWORD
	v_add3_u32 v23, v23, v34, s75
	v_add3_u32 v21, v21, v35, s75
	v_and_b32_e32 v23, 0xffff0000, v23
	v_and_b32_e32 v34, 0xffff0000, v21
	v_or_b32_sdwa v21, v23, v22 dst_sel:DWORD dst_unused:UNUSED_PAD src0_sel:DWORD src1_sel:WORD_1
	v_and_b32_sdwa v23, v8, v236 dst_sel:DWORD dst_unused:UNUSED_PAD src0_sel:WORD_1 src1_sel:DWORD
	v_and_b32_sdwa v22, v10, v236 dst_sel:DWORD dst_unused:UNUSED_PAD src0_sel:WORD_1 src1_sel:DWORD
	v_add3_u32 v8, v8, v23, s75
	v_and_b32_sdwa v23, v9, v236 dst_sel:DWORD dst_unused:UNUSED_PAD src0_sel:WORD_1 src1_sel:DWORD
	v_add3_u32 v10, v10, v22, s75
	v_and_b32_sdwa v22, v11, v236 dst_sel:DWORD dst_unused:UNUSED_PAD src0_sel:WORD_1 src1_sel:DWORD
	v_add3_u32 v9, v9, v23, s75
	v_add3_u32 v11, v11, v22, s75
	v_and_b32_e32 v9, 0xffff0000, v9
	v_and_b32_e32 v11, 0xffff0000, v11
	v_or_b32_sdwa v22, v9, v8 dst_sel:DWORD dst_unused:UNUSED_PAD src0_sel:DWORD src1_sel:WORD_1
	s_waitcnt vmcnt(4)
	v_and_b32_sdwa v9, v24, v236 dst_sel:DWORD dst_unused:UNUSED_PAD src0_sel:WORD_1 src1_sel:DWORD
	v_or_b32_sdwa v23, v11, v10 dst_sel:DWORD dst_unused:UNUSED_PAD src0_sel:DWORD src1_sel:WORD_1
	v_add3_u32 v10, v24, v9, s75
	v_and_b32_sdwa v9, v27, v236 dst_sel:DWORD dst_unused:UNUSED_PAD src0_sel:WORD_1 src1_sel:DWORD
	v_and_b32_sdwa v11, v25, v236 dst_sel:DWORD dst_unused:UNUSED_PAD src0_sel:WORD_1 src1_sel:DWORD
	v_and_b32_sdwa v8, v26, v236 dst_sel:DWORD dst_unused:UNUSED_PAD src0_sel:WORD_1 src1_sel:DWORD
	v_add3_u32 v9, v27, v9, s75
	v_add3_u32 v11, v25, v11, s75
	v_add3_u32 v8, v26, v8, s75
	v_and_b32_e32 v9, 0xffff0000, v9
	v_and_b32_e32 v11, 0xffff0000, v11
	v_or_b32_sdwa v9, v9, v8 dst_sel:DWORD dst_unused:UNUSED_PAD src0_sel:DWORD src1_sel:WORD_1
	v_or_b32_sdwa v8, v11, v10 dst_sel:DWORD dst_unused:UNUSED_PAD src0_sel:DWORD src1_sel:WORD_1
	v_and_b32_sdwa v10, v14, v236 dst_sel:DWORD dst_unused:UNUSED_PAD src0_sel:WORD_1 src1_sel:DWORD
	v_and_b32_sdwa v11, v12, v236 dst_sel:DWORD dst_unused:UNUSED_PAD src0_sel:WORD_1 src1_sel:DWORD
	v_add3_u32 v12, v12, v11, s75
	v_add3_u32 v10, v14, v10, s75
	v_and_b32_sdwa v11, v15, v236 dst_sel:DWORD dst_unused:UNUSED_PAD src0_sel:WORD_1 src1_sel:DWORD
	v_and_b32_sdwa v14, v13, v236 dst_sel:DWORD dst_unused:UNUSED_PAD src0_sel:WORD_1 src1_sel:DWORD
	v_and_b32_e32 v33, 0xffff0000, v33
	v_add3_u32 v11, v15, v11, s75
	v_add3_u32 v13, v13, v14, s75
	v_or_b32_sdwa v38, v33, v32 dst_sel:DWORD dst_unused:UNUSED_PAD src0_sel:DWORD src1_sel:WORD_1
	v_lshl_add_u64 v[32:33], v[60:61], 4, s[96:97]
	v_or_b32_sdwa v20, v34, v20 dst_sel:DWORD dst_unused:UNUSED_PAD src0_sel:DWORD src1_sel:WORD_1
	v_and_b32_e32 v11, 0xffff0000, v11
	v_and_b32_e32 v13, 0xffff0000, v13
	global_store_dwordx4 v[32:33], v[20:23], off
	v_or_b32_sdwa v11, v11, v10 dst_sel:DWORD dst_unused:UNUSED_PAD src0_sel:DWORD src1_sel:WORD_1
	v_or_b32_sdwa v10, v13, v12 dst_sel:DWORD dst_unused:UNUSED_PAD src0_sel:DWORD src1_sel:WORD_1
	v_lshl_add_u64 v[20:21], v[62:63], 4, s[96:97]
	global_store_dwordx4 v[20:21], v[8:11], off
	v_and_b32_sdwa v56, v50, v236 dst_sel:DWORD dst_unused:UNUSED_PAD src0_sel:WORD_1 src1_sel:DWORD
	v_add3_u32 v50, v50, v56, s75
	s_waitcnt vmcnt(4)
	v_and_b32_sdwa v10, v6, v236 dst_sel:DWORD dst_unused:UNUSED_PAD src0_sel:WORD_1 src1_sel:DWORD
	v_and_b32_sdwa v11, v4, v236 dst_sel:DWORD dst_unused:UNUSED_PAD src0_sel:WORD_1 src1_sel:DWORD
	v_add3_u32 v6, v6, v10, s75
	v_and_b32_sdwa v10, v7, v236 dst_sel:DWORD dst_unused:UNUSED_PAD src0_sel:WORD_1 src1_sel:DWORD
	v_add3_u32 v4, v4, v11, s75
	v_and_b32_sdwa v11, v5, v236 dst_sel:DWORD dst_unused:UNUSED_PAD src0_sel:WORD_1 src1_sel:DWORD
	v_add3_u32 v7, v7, v10, s75
	v_add3_u32 v5, v5, v11, s75
	v_and_b32_e32 v7, 0xffff0000, v7
	v_and_b32_e32 v10, 0xffff0000, v5
	v_or_b32_sdwa v5, v7, v6 dst_sel:DWORD dst_unused:UNUSED_PAD src0_sel:DWORD src1_sel:WORD_1
	v_and_b32_sdwa v7, v0, v236 dst_sel:DWORD dst_unused:UNUSED_PAD src0_sel:WORD_1 src1_sel:DWORD
	v_and_b32_sdwa v6, v2, v236 dst_sel:DWORD dst_unused:UNUSED_PAD src0_sel:WORD_1 src1_sel:DWORD
	v_add3_u32 v0, v0, v7, s75
	v_and_b32_sdwa v7, v1, v236 dst_sel:DWORD dst_unused:UNUSED_PAD src0_sel:WORD_1 src1_sel:DWORD
	v_add3_u32 v2, v2, v6, s75
	v_and_b32_sdwa v6, v3, v236 dst_sel:DWORD dst_unused:UNUSED_PAD src0_sel:WORD_1 src1_sel:DWORD
	v_add3_u32 v1, v1, v7, s75
	v_add3_u32 v3, v3, v6, s75
	v_and_b32_e32 v1, 0xffff0000, v1
	v_and_b32_e32 v3, 0xffff0000, v3
	v_or_b32_sdwa v6, v1, v0 dst_sel:DWORD dst_unused:UNUSED_PAD src0_sel:DWORD src1_sel:WORD_1
	s_waitcnt vmcnt(2)
	v_and_b32_sdwa v1, v28, v236 dst_sel:DWORD dst_unused:UNUSED_PAD src0_sel:WORD_1 src1_sel:DWORD
	v_or_b32_sdwa v7, v3, v2 dst_sel:DWORD dst_unused:UNUSED_PAD src0_sel:DWORD src1_sel:WORD_1
	v_add3_u32 v2, v28, v1, s75
	v_and_b32_sdwa v1, v31, v236 dst_sel:DWORD dst_unused:UNUSED_PAD src0_sel:WORD_1 src1_sel:DWORD
	v_and_b32_sdwa v3, v29, v236 dst_sel:DWORD dst_unused:UNUSED_PAD src0_sel:WORD_1 src1_sel:DWORD
	v_and_b32_sdwa v0, v30, v236 dst_sel:DWORD dst_unused:UNUSED_PAD src0_sel:WORD_1 src1_sel:DWORD
	v_add3_u32 v1, v31, v1, s75
	v_add3_u32 v3, v29, v3, s75
	v_add3_u32 v0, v30, v0, s75
	v_and_b32_e32 v1, 0xffff0000, v1
	v_and_b32_e32 v3, 0xffff0000, v3
	v_and_b32_sdwa v56, v51, v236 dst_sel:DWORD dst_unused:UNUSED_PAD src0_sel:WORD_1 src1_sel:DWORD
	v_lshl_add_u64 v[8:9], v[58:59], 4, s[96:97]
	v_or_b32_sdwa v4, v10, v4 dst_sel:DWORD dst_unused:UNUSED_PAD src0_sel:DWORD src1_sel:WORD_1
	v_or_b32_sdwa v1, v1, v0 dst_sel:DWORD dst_unused:UNUSED_PAD src0_sel:DWORD src1_sel:WORD_1
	v_or_b32_sdwa v0, v3, v2 dst_sel:DWORD dst_unused:UNUSED_PAD src0_sel:DWORD src1_sel:WORD_1
	v_and_b32_sdwa v3, v16, v236 dst_sel:DWORD dst_unused:UNUSED_PAD src0_sel:WORD_1 src1_sel:DWORD
	v_add3_u32 v51, v51, v56, s75
	global_store_dwordx4 v[8:9], v[4:7], off
	v_and_b32_e32 v51, 0xffff0000, v51
	v_and_b32_sdwa v2, v18, v236 dst_sel:DWORD dst_unused:UNUSED_PAD src0_sel:WORD_1 src1_sel:DWORD
	v_add3_u32 v6, v16, v3, s75
	v_and_b32_sdwa v3, v19, v236 dst_sel:DWORD dst_unused:UNUSED_PAD src0_sel:WORD_1 src1_sel:DWORD
	v_and_b32_sdwa v7, v17, v236 dst_sel:DWORD dst_unused:UNUSED_PAD src0_sel:WORD_1 src1_sel:DWORD
	v_add3_u32 v3, v19, v3, s75
	v_add3_u32 v7, v17, v7, s75
	v_or_b32_sdwa v56, v51, v50 dst_sel:DWORD dst_unused:UNUSED_PAD src0_sel:DWORD src1_sel:WORD_1
	v_lshl_add_u64 v[50:51], v[68:69], 4, s[96:97]
	v_or_b32_sdwa v44, v49, v44 dst_sel:DWORD dst_unused:UNUSED_PAD src0_sel:DWORD src1_sel:WORD_1
	v_add3_u32 v2, v18, v2, s75
	v_and_b32_e32 v3, 0xffff0000, v3
	v_and_b32_e32 v7, 0xffff0000, v7
	global_store_dwordx4 v[50:51], v[44:47], off
	v_lshl_add_u64 v[4:5], v[64:65], 4, s[96:97]
	v_or_b32_sdwa v3, v3, v2 dst_sel:DWORD dst_unused:UNUSED_PAD src0_sel:DWORD src1_sel:WORD_1
	v_lshl_add_u64 v[44:45], v[66:67], 4, s[96:97]
	v_or_b32_sdwa v2, v7, v6 dst_sel:DWORD dst_unused:UNUSED_PAD src0_sel:DWORD src1_sel:WORD_1
	global_store_dwordx4 v[80:81], v[76:79], off
	global_store_dwordx4 v[70:71], v[54:57], off
	global_store_dwordx4 v[44:45], v[36:39], off
	global_store_dwordx4 v[4:5], v[0:3], off

.LBB0_916:
	s_setprio 0
	v_readlane_b32 s1, v255, 38
	s_mul_i32 s1, s1, 13
	v_readlane_b32 s92, v254, 3
	s_add_i32 s1, s1, 5
	v_readlane_b32 s93, v254, 4
	s_cmp_lt_i32 s1, s93
	v_readlane_b32 s56, v255, 24
	s_cselect_b64 s[4:5], -1, 0
	v_readlane_b32 s57, v255, 25
	s_and_b64 s[4:5], s[56:57], s[4:5]
	s_andn2_b64 vcc, exec, s[4:5]
	v_readlane_b32 s94, v254, 5
	v_readlane_b32 s95, v254, 6
	s_cbranch_vccnz .LBB0_928
	s_waitcnt vmcnt(0)
	v_readlane_b32 s4, v254, 9
	v_cmp_eq_u32_e32 vcc, 0, v234
	v_readlane_b32 s5, v254, 10
	s_and_b64 s[6:7], s[4:5], vcc
	s_barrier
	s_and_saveexec_b64 s[4:5], s[6:7]
	v_readlane_b32 s54, v255, 22
	v_readlane_b32 s88, v255, 26
	v_readlane_b32 s90, v255, 28
	v_readlane_b32 s55, v255, 23
	v_readlane_b32 s89, v255, 27
	v_readlane_b32 s91, v255, 29
	s_mov_b64 s[78:79], 0x800
	s_mov_b64 s[96:97], 0x50000
	v_readlane_b32 s26, v255, 41
	s_cbranch_execz .LBB0_966
	v_readlane_b32 s6, v254, 2
	s_waitcnt vmcnt(0) expcnt(0) lgkmcnt(0)
	s_nop 0
	v_mov_b32_e32 v0, s6
	ds_read_b32 v2, v0
	ds_read_b32 v0, v0 offset:4
	s_waitcnt lgkmcnt(1)
	v_cmp_ne_u32_e32 vcc, 0, v2
	s_cbranch_vccnz .LBB0_934
	v_readlane_b32 s8, v254, 0
	v_readlane_b32 s9, v254, 1
	s_load_dwordx2 s[6:7], s[8:9], 0x4
	s_mov_b32 s17, 1
	s_waitcnt lgkmcnt(0)
	s_mul_i32 s12, s6, s76
	s_mul_i32 s12, s12, s7
	s_branch .LBB0_921
